# candidate ranking loops: compare results alternate between two SGPR pairs, one pad per two compares instead of a two-state pad per compare
# baseline (speedup 1.0000x reference)
; #define LAS __attribute__((address_space(3)))
; #define LDS_WAIT() asm volatile("s_waitcnt lgkmcnt(0)" ::: "memory")
; template <int NC> __device__ __forceinline__ void idx_rank(LAS unsigned long long* cc, int n, unsigned nd, int lane, LAS unsigned* mrow) {
;     const int n8 = (n + 7) & ~7;
;     if (lane < 7 && n + lane < n8) { unsigned z; asm volatile("v_mov_b32 %0, 0" : "=v"(z)); ((LAS unsigned*)cc)[2 * (n + lane)] = z; ((LAS unsigned*)cc)[2 * (n + lane) + 1] = z; }
;     LDS_WAIT();
;     unsigned long long me[NC]; unsigned rank[NC];
; #pragma unroll
;     for (int k = 0; k < NC; ++k) { me[k] = (lane + 64 * k < n) ? cc[lane + 64 * k] : ~0ull; rank[k] = 0u; }
; #pragma unroll 2
;     for (int c2 = 0; c2 < n8; c2 += 8) {
;         unsigned long long a[8];
; #pragma unroll
;         for (int i = 0; i < 8; ++i) a[i] = cc[c2 + i];
; #pragma unroll
;         for (int i = 0; i < 8; ++i)
; #pragma unroll
;             for (int k = 0; k < NC; ++k) rank[k] += (a[i] > me[k]) ? 1u : 0u;
;     }
.LBB0_1343:
	s_waitcnt vmcnt(0)
	v_mov_b32_e32 v32, s33
	ds_read_b128 v[16:19], v32
	ds_read_b128 v[20:23], v32 offset:16
	ds_read_b128 v[24:27], v32 offset:32
	ds_read_b128 v[28:31], v32 offset:48
	s_add_i32 s2, s2, 16
	s_waitcnt lgkmcnt(3)
	s_addk_i32 s33, 0x80
	s_add_i32 s3, s3, -2
	s_cmp_lg_u32 s3, 0
	v_cmp_gt_u64_e64 s[16:17], v[16:17], v[8:9]
	v_cmp_gt_u64_e64 s[100:101], v[16:17], v[4:5]
	s_nop 0
	v_cndmask_b32_e64 v15, 0, 1, s[16:17]
	v_cndmask_b32_e64 v33, 0, 1, s[100:101]
	v_cmp_gt_u64_e64 s[16:17], v[16:17], v[6:7]
	v_cmp_gt_u64_e64 s[100:101], v[18:19], v[8:9]
	s_nop 0
	v_cndmask_b32_e64 v16, 0, 1, s[16:17]
	v_addc_co_u32_e64 v14, s[100:101], v14, v15, s[100:101]
	v_cmp_gt_u64_e64 s[16:17], v[18:19], v[4:5]
	v_cmp_gt_u64_e64 s[100:101], v[18:19], v[6:7]
	s_nop 0
	v_addc_co_u32_e64 v13, s[16:17], v13, v33, s[16:17]
	v_addc_co_u32_e64 v3, s[100:101], v3, v16, s[100:101]
	s_waitcnt lgkmcnt(2)
	v_cmp_gt_u64_e64 s[16:17], v[20:21], v[8:9]
	v_cmp_gt_u64_e64 s[100:101], v[20:21], v[4:5]
	s_nop 0
	v_cndmask_b32_e64 v15, 0, 1, s[16:17]
	v_cndmask_b32_e64 v16, 0, 1, s[100:101]
	v_cmp_gt_u64_e64 s[16:17], v[20:21], v[6:7]
	v_cmp_gt_u64_e64 s[100:101], v[22:23], v[8:9]
	s_nop 0
	v_cndmask_b32_e64 v17, 0, 1, s[16:17]
	v_addc_co_u32_e64 v14, s[100:101], v14, v15, s[100:101]
	v_cmp_gt_u64_e64 s[16:17], v[22:23], v[4:5]
	v_cmp_gt_u64_e64 s[100:101], v[22:23], v[6:7]
	s_nop 0
	v_addc_co_u32_e64 v13, s[16:17], v13, v16, s[16:17]
	v_addc_co_u32_e64 v3, s[100:101], v3, v17, s[100:101]
	s_waitcnt lgkmcnt(1)
	v_cmp_gt_u64_e64 s[16:17], v[24:25], v[8:9]
	v_cmp_gt_u64_e64 s[100:101], v[24:25], v[4:5]
	s_nop 0
	v_cndmask_b32_e64 v15, 0, 1, s[16:17]
	v_cndmask_b32_e64 v16, 0, 1, s[100:101]
	v_cmp_gt_u64_e64 s[16:17], v[24:25], v[6:7]
	v_cmp_gt_u64_e64 s[100:101], v[26:27], v[8:9]
	s_nop 0
	v_cndmask_b32_e64 v17, 0, 1, s[16:17]
	v_addc_co_u32_e64 v14, s[100:101], v14, v15, s[100:101]
	v_cmp_gt_u64_e64 s[16:17], v[26:27], v[4:5]
	v_cmp_gt_u64_e64 s[100:101], v[26:27], v[6:7]
	s_nop 0
	v_addc_co_u32_e64 v13, s[16:17], v13, v16, s[16:17]
	v_addc_co_u32_e64 v3, s[100:101], v3, v17, s[100:101]
	s_waitcnt lgkmcnt(0)
	v_cmp_gt_u64_e64 s[16:17], v[28:29], v[8:9]
	v_cmp_gt_u64_e64 s[100:101], v[28:29], v[4:5]
	s_nop 0
	v_cndmask_b32_e64 v15, 0, 1, s[16:17]
	v_cndmask_b32_e64 v16, 0, 1, s[100:101]
	v_cmp_gt_u64_e64 s[16:17], v[28:29], v[6:7]
	v_cmp_gt_u64_e64 s[100:101], v[30:31], v[8:9]
	s_nop 0
	v_cndmask_b32_e64 v17, 0, 1, s[16:17]
	v_addc_co_u32_e64 v33, s[100:101], v14, v15, s[100:101]
	v_cmp_gt_u64_e64 s[16:17], v[30:31], v[4:5]
	v_cmp_gt_u64_e64 s[100:101], v[30:31], v[6:7]
	s_nop 0
	v_addc_co_u32_e64 v13, s[16:17], v13, v16, s[16:17]
	v_addc_co_u32_e64 v3, s[100:101], v3, v17, s[100:101]
	ds_read_b128 v[14:17], v32 offset:64
	ds_read_b128 v[18:21], v32 offset:80
	ds_read_b128 v[22:25], v32 offset:96
	ds_read_b128 v[26:29], v32 offset:112
	s_waitcnt lgkmcnt(3)
	v_cmp_gt_u64_e64 s[16:17], v[14:15], v[8:9]
	v_cmp_gt_u64_e64 s[100:101], v[14:15], v[4:5]
	s_nop 0
	v_cndmask_b32_e64 v30, 0, 1, s[16:17]
	v_cndmask_b32_e64 v31, 0, 1, s[100:101]
	v_cmp_gt_u64_e64 s[16:17], v[14:15], v[6:7]
	v_cmp_gt_u64_e64 s[100:101], v[16:17], v[8:9]
	s_nop 0
	v_cndmask_b32_e64 v14, 0, 1, s[16:17]
	v_addc_co_u32_e64 v15, s[100:101], v33, v30, s[100:101]
	v_cmp_gt_u64_e64 s[16:17], v[16:17], v[4:5]
	v_cmp_gt_u64_e64 s[100:101], v[16:17], v[6:7]
	s_nop 0
	v_addc_co_u32_e64 v13, s[16:17], v13, v31, s[16:17]
	v_addc_co_u32_e64 v3, s[100:101], v3, v14, s[100:101]
	s_waitcnt lgkmcnt(2)
	v_cmp_gt_u64_e64 s[16:17], v[18:19], v[8:9]
	v_cmp_gt_u64_e64 s[100:101], v[18:19], v[4:5]
	s_nop 0
	v_cndmask_b32_e64 v14, 0, 1, s[16:17]
	v_cndmask_b32_e64 v16, 0, 1, s[100:101]
	v_cmp_gt_u64_e64 s[16:17], v[18:19], v[6:7]
	v_cmp_gt_u64_e64 s[100:101], v[20:21], v[8:9]
	s_nop 0
	v_cndmask_b32_e64 v17, 0, 1, s[16:17]
	v_addc_co_u32_e64 v14, s[100:101], v15, v14, s[100:101]
	v_cmp_gt_u64_e64 s[16:17], v[20:21], v[4:5]
	v_cmp_gt_u64_e64 s[100:101], v[20:21], v[6:7]
	s_nop 0
	v_addc_co_u32_e64 v13, s[16:17], v13, v16, s[16:17]
	v_addc_co_u32_e64 v3, s[100:101], v3, v17, s[100:101]
	s_waitcnt lgkmcnt(1)
	v_cmp_gt_u64_e64 s[16:17], v[22:23], v[8:9]
	v_cmp_gt_u64_e64 s[100:101], v[22:23], v[4:5]
	s_nop 0
	v_cndmask_b32_e64 v15, 0, 1, s[16:17]
	v_cndmask_b32_e64 v16, 0, 1, s[100:101]
	v_cmp_gt_u64_e64 s[16:17], v[22:23], v[6:7]
	v_cmp_gt_u64_e64 s[100:101], v[24:25], v[8:9]
	s_nop 0
	v_cndmask_b32_e64 v17, 0, 1, s[16:17]
	v_addc_co_u32_e64 v14, s[100:101], v14, v15, s[100:101]
	v_cmp_gt_u64_e64 s[16:17], v[24:25], v[4:5]
	v_cmp_gt_u64_e64 s[100:101], v[24:25], v[6:7]
	s_nop 0
	v_addc_co_u32_e64 v13, s[16:17], v13, v16, s[16:17]
	v_addc_co_u32_e64 v3, s[100:101], v3, v17, s[100:101]
	s_waitcnt lgkmcnt(0)
	v_cmp_gt_u64_e64 s[16:17], v[26:27], v[8:9]
	v_cmp_gt_u64_e64 s[100:101], v[26:27], v[4:5]
	s_nop 0
	v_cndmask_b32_e64 v15, 0, 1, s[16:17]
	v_cndmask_b32_e64 v16, 0, 1, s[100:101]
	v_cmp_gt_u64_e64 s[16:17], v[26:27], v[6:7]
	v_cmp_gt_u64_e64 s[100:101], v[28:29], v[8:9]
	s_nop 0
	v_cndmask_b32_e64 v17, 0, 1, s[16:17]
	v_addc_co_u32_e64 v14, s[100:101], v14, v15, s[100:101]
	v_cmp_gt_u64_e64 s[16:17], v[28:29], v[4:5]
	v_cmp_gt_u64_e64 s[100:101], v[28:29], v[6:7]
	s_nop 0
	v_addc_co_u32_e64 v13, s[16:17], v13, v16, s[16:17]
	v_addc_co_u32_e64 v3, s[100:101], v3, v17, s[100:101]
	s_cbranch_scc1 .LBB0_1343
	s_bitcmp1_b32 s1, 3
	s_cbranch_scc0 .LBB0_1347
	s_branch .LBB0_1348

; template <int NC> __device__ __forceinline__ void idx_rank(LAS unsigned long long* cc, int n, unsigned nd, int lane, LAS unsigned* mrow) {
;     ...
; #pragma unroll 2
;     for (int c2 = 0; c2 < n8; c2 += 8) {
;         unsigned long long a[8];
; #pragma unroll
;         for (int i = 0; i < 8; ++i) a[i] = cc[c2 + i];
; #pragma unroll
;         for (int i = 0; i < 8; ++i)
; #pragma unroll
;             for (int k = 0; k < NC; ++k) rank[k] += (a[i] > me[k]) ? 1u : 0u;
;     }
.LBB0_1347:
	s_lshl_b32 s1, s2, 3
	s_add_i32 s1, s19, s1
	v_mov_b32_e32 v15, s1
	s_waitcnt vmcnt(3)
	ds_read_b128 v[16:19], v15 offset:512
	s_waitcnt vmcnt(2)
	ds_read_b128 v[20:23], v15 offset:528
	s_waitcnt vmcnt(1)
	ds_read_b128 v[24:27], v15 offset:544
	s_waitcnt vmcnt(0)
	ds_read_b128 v[28:31], v15 offset:560
	s_waitcnt lgkmcnt(3)
	v_cmp_gt_u64_e64 s[16:17], v[16:17], v[8:9]
	v_cmp_gt_u64_e64 s[100:101], v[16:17], v[4:5]
	s_nop 0
	v_cndmask_b32_e64 v15, 0, 1, s[16:17]
	v_cndmask_b32_e64 v32, 0, 1, s[100:101]
	v_cmp_gt_u64_e64 s[16:17], v[16:17], v[6:7]
	v_cmp_gt_u64_e64 s[100:101], v[18:19], v[8:9]
	s_nop 0
	v_cndmask_b32_e64 v16, 0, 1, s[16:17]
	v_addc_co_u32_e64 v14, s[100:101], v14, v15, s[100:101]
	v_cmp_gt_u64_e64 s[16:17], v[18:19], v[4:5]
	v_cmp_gt_u64_e64 s[100:101], v[18:19], v[6:7]
	s_nop 0
	v_addc_co_u32_e64 v13, s[16:17], v13, v32, s[16:17]
	v_addc_co_u32_e64 v3, s[100:101], v3, v16, s[100:101]
	s_waitcnt lgkmcnt(2)
	v_cmp_gt_u64_e64 s[16:17], v[20:21], v[8:9]
	v_cmp_gt_u64_e64 s[100:101], v[20:21], v[4:5]
	s_nop 0
	v_cndmask_b32_e64 v15, 0, 1, s[16:17]
	v_cndmask_b32_e64 v16, 0, 1, s[100:101]
	v_cmp_gt_u64_e64 s[16:17], v[20:21], v[6:7]
	v_cmp_gt_u64_e64 s[100:101], v[22:23], v[8:9]
	s_nop 0
	v_cndmask_b32_e64 v17, 0, 1, s[16:17]
	v_addc_co_u32_e64 v14, s[100:101], v14, v15, s[100:101]
	v_cmp_gt_u64_e64 s[16:17], v[22:23], v[4:5]
	v_cmp_gt_u64_e64 s[100:101], v[22:23], v[6:7]
	s_nop 0
	v_addc_co_u32_e64 v13, s[16:17], v13, v16, s[16:17]
	v_addc_co_u32_e64 v3, s[100:101], v3, v17, s[100:101]
	s_waitcnt lgkmcnt(1)
	v_cmp_gt_u64_e64 s[16:17], v[24:25], v[8:9]
	v_cmp_gt_u64_e64 s[100:101], v[24:25], v[4:5]
	s_nop 0
	v_cndmask_b32_e64 v15, 0, 1, s[16:17]
	v_cndmask_b32_e64 v16, 0, 1, s[100:101]
	v_cmp_gt_u64_e64 s[16:17], v[24:25], v[6:7]
	v_cmp_gt_u64_e64 s[100:101], v[26:27], v[8:9]
	s_nop 0
	v_cndmask_b32_e64 v17, 0, 1, s[16:17]
	v_addc_co_u32_e64 v14, s[100:101], v14, v15, s[100:101]
	v_cmp_gt_u64_e64 s[16:17], v[26:27], v[4:5]
	v_cmp_gt_u64_e64 s[100:101], v[26:27], v[6:7]
	s_nop 0
	v_addc_co_u32_e64 v13, s[16:17], v13, v16, s[16:17]
	v_addc_co_u32_e64 v3, s[100:101], v3, v17, s[100:101]
	s_waitcnt lgkmcnt(0)
	v_cmp_gt_u64_e64 s[16:17], v[28:29], v[8:9]
	v_cmp_gt_u64_e64 s[100:101], v[28:29], v[4:5]
	s_nop 0
	v_cndmask_b32_e64 v15, 0, 1, s[16:17]
	v_cndmask_b32_e64 v16, 0, 1, s[100:101]
	v_cmp_gt_u64_e64 s[16:17], v[28:29], v[6:7]
	v_cmp_gt_u64_e64 s[100:101], v[30:31], v[8:9]
	s_nop 0
	v_cndmask_b32_e64 v17, 0, 1, s[16:17]
	v_addc_co_u32_e64 v14, s[100:101], v14, v15, s[100:101]
	v_cmp_gt_u64_e64 s[16:17], v[30:31], v[4:5]
	v_cmp_gt_u64_e64 s[100:101], v[30:31], v[6:7]
	s_nop 0
	v_addc_co_u32_e64 v13, s[16:17], v13, v16, s[16:17]
	v_addc_co_u32_e64 v3, s[100:101], v3, v17, s[100:101]

; template <int NC> __device__ __forceinline__ void idx_rank(LAS unsigned long long* cc, int n, unsigned nd, int lane, LAS unsigned* mrow) {
;     ...
; #pragma unroll 2
;     for (int c2 = 0; c2 < n8; c2 += 8) {
;         unsigned long long a[8];
; #pragma unroll
;         for (int i = 0; i < 8; ++i) a[i] = cc[c2 + i];
; #pragma unroll
;         for (int i = 0; i < 8; ++i)
; #pragma unroll
;             for (int k = 0; k < NC; ++k) rank[k] += (a[i] > me[k]) ? 1u : 0u;
;     }
.LBB0_1364:
	v_mov_b32_e32 v9, s3
	ds_read_b128 v[14:17], v9
	s_waitcnt vmcnt(3)
	ds_read_b128 v[18:21], v9 offset:16
	s_waitcnt vmcnt(2)
	ds_read_b128 v[22:25], v9 offset:32
	s_waitcnt vmcnt(1)
	ds_read_b128 v[26:29], v9 offset:48
	s_add_i32 s1, s1, 16
	s_waitcnt lgkmcnt(3)
	s_addk_i32 s3, 0x80
	s_add_i32 s2, s2, -2
	s_cmp_lg_u32 s2, 0
	v_cmp_gt_u64_e64 s[14:15], v[14:15], v[6:7]
	v_cmp_gt_u64_e64 s[100:101], v[14:15], v[4:5]
	s_nop 0
	v_cndmask_b32_e64 v13, 0, 1, s[14:15]
	v_cndmask_b32_e64 v14, 0, 1, s[100:101]
	v_cmp_gt_u64_e64 s[14:15], v[16:17], v[6:7]
	v_cmp_gt_u64_e64 s[100:101], v[16:17], v[4:5]
	s_nop 0
	v_addc_co_u32_e64 v8, s[14:15], v8, v13, s[14:15]
	v_addc_co_u32_e64 v3, s[100:101], v3, v14, s[100:101]
	s_waitcnt lgkmcnt(2)
	v_cmp_gt_u64_e64 s[14:15], v[18:19], v[6:7]
	v_cmp_gt_u64_e64 s[100:101], v[18:19], v[4:5]
	s_nop 0
	v_cndmask_b32_e64 v13, 0, 1, s[14:15]
	v_cndmask_b32_e64 v14, 0, 1, s[100:101]
	v_cmp_gt_u64_e64 s[14:15], v[20:21], v[6:7]
	v_cmp_gt_u64_e64 s[100:101], v[20:21], v[4:5]
	s_nop 0
	v_addc_co_u32_e64 v8, s[14:15], v8, v13, s[14:15]
	v_addc_co_u32_e64 v3, s[100:101], v3, v14, s[100:101]
	s_waitcnt lgkmcnt(1)
	v_cmp_gt_u64_e64 s[14:15], v[22:23], v[6:7]
	v_cmp_gt_u64_e64 s[100:101], v[22:23], v[4:5]
	s_nop 0
	v_cndmask_b32_e64 v13, 0, 1, s[14:15]
	v_cndmask_b32_e64 v14, 0, 1, s[100:101]
	v_cmp_gt_u64_e64 s[14:15], v[24:25], v[6:7]
	v_cmp_gt_u64_e64 s[100:101], v[24:25], v[4:5]
	s_nop 0
	v_addc_co_u32_e64 v8, s[14:15], v8, v13, s[14:15]
	v_addc_co_u32_e64 v3, s[100:101], v3, v14, s[100:101]
	s_waitcnt lgkmcnt(0)
	v_cmp_gt_u64_e64 s[14:15], v[26:27], v[6:7]
	v_cmp_gt_u64_e64 s[100:101], v[26:27], v[4:5]
	s_nop 0
	v_cndmask_b32_e64 v13, 0, 1, s[14:15]
	v_cndmask_b32_e64 v14, 0, 1, s[100:101]
	v_cmp_gt_u64_e64 s[14:15], v[28:29], v[6:7]
	v_cmp_gt_u64_e64 s[100:101], v[28:29], v[4:5]
	s_nop 0
	v_addc_co_u32_e64 v8, s[14:15], v8, v13, s[14:15]
	v_addc_co_u32_e64 v3, s[100:101], v3, v14, s[100:101]
	ds_read_b128 v[14:17], v9 offset:64
	ds_read_b128 v[18:21], v9 offset:80
	ds_read_b128 v[22:25], v9 offset:96
	ds_read_b128 v[26:29], v9 offset:112
	s_waitcnt lgkmcnt(3)
	v_cmp_gt_u64_e64 s[14:15], v[14:15], v[6:7]
	v_cmp_gt_u64_e64 s[100:101], v[14:15], v[4:5]
	s_nop 0
	v_cndmask_b32_e64 v9, 0, 1, s[14:15]
	v_cndmask_b32_e64 v13, 0, 1, s[100:101]
	v_cmp_gt_u64_e64 s[14:15], v[16:17], v[6:7]
	v_cmp_gt_u64_e64 s[100:101], v[16:17], v[4:5]
	s_nop 0
	v_addc_co_u32_e64 v8, s[14:15], v8, v9, s[14:15]
	v_addc_co_u32_e64 v3, s[100:101], v3, v13, s[100:101]
	s_waitcnt lgkmcnt(2)
	v_cmp_gt_u64_e64 s[14:15], v[18:19], v[6:7]
	v_cmp_gt_u64_e64 s[100:101], v[18:19], v[4:5]
	s_nop 0
	v_cndmask_b32_e64 v9, 0, 1, s[14:15]
	v_cndmask_b32_e64 v13, 0, 1, s[100:101]
	v_cmp_gt_u64_e64 s[14:15], v[20:21], v[6:7]
	v_cmp_gt_u64_e64 s[100:101], v[20:21], v[4:5]
	s_nop 0
	v_addc_co_u32_e64 v8, s[14:15], v8, v9, s[14:15]
	v_addc_co_u32_e64 v3, s[100:101], v3, v13, s[100:101]
	s_waitcnt lgkmcnt(1)
	v_cmp_gt_u64_e64 s[14:15], v[22:23], v[6:7]
	v_cmp_gt_u64_e64 s[100:101], v[22:23], v[4:5]
	s_nop 0
	v_cndmask_b32_e64 v9, 0, 1, s[14:15]
	v_cndmask_b32_e64 v13, 0, 1, s[100:101]
	v_cmp_gt_u64_e64 s[14:15], v[24:25], v[6:7]
	v_cmp_gt_u64_e64 s[100:101], v[24:25], v[4:5]
	s_nop 0
	v_addc_co_u32_e64 v8, s[14:15], v8, v9, s[14:15]
	v_addc_co_u32_e64 v3, s[100:101], v3, v13, s[100:101]
	s_waitcnt lgkmcnt(0)
	v_cmp_gt_u64_e64 s[14:15], v[26:27], v[6:7]
	v_cmp_gt_u64_e64 s[100:101], v[26:27], v[4:5]
	s_nop 0
	v_cndmask_b32_e64 v9, 0, 1, s[14:15]
	v_cndmask_b32_e64 v13, 0, 1, s[100:101]
	v_cmp_gt_u64_e64 s[14:15], v[28:29], v[6:7]
	v_cmp_gt_u64_e64 s[100:101], v[28:29], v[4:5]
	s_nop 0
	v_addc_co_u32_e64 v8, s[14:15], v8, v9, s[14:15]
	v_addc_co_u32_e64 v3, s[100:101], v3, v13, s[100:101]
	s_cbranch_scc1 .LBB0_1364
	s_bitcmp1_b32 s0, 3
	s_cbranch_scc0 .LBB0_1417
	s_branch .LBB0_1418

; template <int NC> __device__ __forceinline__ void idx_rank(LAS unsigned long long* cc, int n, unsigned nd, int lane, LAS unsigned* mrow) {
;     ...
; #pragma unroll 2
;     for (int c2 = 0; c2 < n8; c2 += 8) {
;         unsigned long long a[8];
; #pragma unroll
;         for (int i = 0; i < 8; ++i) a[i] = cc[c2 + i];
; #pragma unroll
;         for (int i = 0; i < 8; ++i)
; #pragma unroll
;             for (int k = 0; k < NC; ++k) rank[k] += (a[i] > me[k]) ? 1u : 0u;
;     }
.LBB0_1376:
	v_mov_b32_e32 v13, s3
	ds_read_b128 v[6:9], v13
	ds_read_b128 v[14:17], v13 offset:16
	s_waitcnt vmcnt(3)
	ds_read_b128 v[18:21], v13 offset:32
	s_waitcnt vmcnt(2)
	ds_read_b128 v[22:25], v13 offset:48
	s_add_i32 s1, s1, 16
	s_waitcnt lgkmcnt(3)
	s_addk_i32 s3, 0x80
	s_add_i32 s2, s2, -2
	s_cmp_lg_u32 s2, 0
	v_cmp_gt_u64_e64 s[12:13], v[6:7], v[4:5]
	v_cmp_gt_u64_e64 s[100:101], v[8:9], v[4:5]
	s_nop 0
	v_cndmask_b32_e64 v6, 0, 1, s[12:13]
	v_addc_co_u32_e64 v3, s[100:101], v3, v6, s[100:101]
	s_waitcnt lgkmcnt(2)
	v_cmp_gt_u64_e64 s[12:13], v[14:15], v[4:5]
	v_cmp_gt_u64_e64 s[100:101], v[16:17], v[4:5]
	s_nop 0
	v_cndmask_b32_e64 v6, 0, 1, s[12:13]
	v_addc_co_u32_e64 v3, s[100:101], v3, v6, s[100:101]
	s_waitcnt lgkmcnt(1)
	v_cmp_gt_u64_e64 s[12:13], v[18:19], v[4:5]
	v_cmp_gt_u64_e64 s[100:101], v[20:21], v[4:5]
	s_nop 0
	v_cndmask_b32_e64 v6, 0, 1, s[12:13]
	v_addc_co_u32_e64 v3, s[100:101], v3, v6, s[100:101]
	s_waitcnt lgkmcnt(0)
	v_cmp_gt_u64_e64 s[12:13], v[22:23], v[4:5]
	v_cmp_gt_u64_e64 s[100:101], v[24:25], v[4:5]
	s_nop 0
	v_cndmask_b32_e64 v6, 0, 1, s[12:13]
	v_addc_co_u32_e64 v3, s[100:101], v3, v6, s[100:101]
	ds_read_b128 v[6:9], v13 offset:64
	ds_read_b128 v[14:17], v13 offset:80
	ds_read_b128 v[18:21], v13 offset:96
	ds_read_b128 v[22:25], v13 offset:112
	s_waitcnt lgkmcnt(3)
	v_cmp_gt_u64_e64 s[12:13], v[6:7], v[4:5]
	v_cmp_gt_u64_e64 s[100:101], v[8:9], v[4:5]
	s_nop 0
	v_cndmask_b32_e64 v6, 0, 1, s[12:13]
	v_addc_co_u32_e64 v3, s[100:101], v3, v6, s[100:101]
	s_waitcnt lgkmcnt(2)
	v_cmp_gt_u64_e64 s[12:13], v[14:15], v[4:5]
	v_cmp_gt_u64_e64 s[100:101], v[16:17], v[4:5]
	s_nop 0
	v_cndmask_b32_e64 v6, 0, 1, s[12:13]
	v_addc_co_u32_e64 v3, s[100:101], v3, v6, s[100:101]
	s_waitcnt lgkmcnt(1)
	v_cmp_gt_u64_e64 s[12:13], v[18:19], v[4:5]
	v_cmp_gt_u64_e64 s[100:101], v[20:21], v[4:5]
	s_nop 0
	v_cndmask_b32_e64 v6, 0, 1, s[12:13]
	v_addc_co_u32_e64 v3, s[100:101], v3, v6, s[100:101]
	s_waitcnt lgkmcnt(0)
	v_cmp_gt_u64_e64 s[12:13], v[22:23], v[4:5]
	v_cmp_gt_u64_e64 s[100:101], v[24:25], v[4:5]
	s_nop 0
	v_cndmask_b32_e64 v6, 0, 1, s[12:13]
	v_addc_co_u32_e64 v3, s[100:101], v3, v6, s[100:101]
	s_cbranch_scc1 .LBB0_1376
	s_bitcmp1_b32 s0, 3
	s_cbranch_scc0 .LBB0_1383
	s_branch .LBB0_1384

; template <int NC> __device__ __forceinline__ void idx_rank(LAS unsigned long long* cc, int n, unsigned nd, int lane, LAS unsigned* mrow) {
;     ...
; #pragma unroll 2
;     for (int c2 = 0; c2 < n8; c2 += 8) {
;         unsigned long long a[8];
; #pragma unroll
;         for (int i = 0; i < 8; ++i) a[i] = cc[c2 + i];
; #pragma unroll
;         for (int i = 0; i < 8; ++i)
; #pragma unroll
;             for (int k = 0; k < NC; ++k) rank[k] += (a[i] > me[k]) ? 1u : 0u;
;     }
.LBB0_1383:
	s_lshl_b32 s0, s1, 3
	s_add_i32 s0, s19, s0
	v_mov_b32_e32 v13, s0
	ds_read_b128 v[6:9], v13 offset:512
	ds_read_b128 v[14:17], v13 offset:528
	s_waitcnt vmcnt(3)
	ds_read_b128 v[18:21], v13 offset:544
	s_waitcnt vmcnt(2)
	ds_read_b128 v[22:25], v13 offset:560
	s_waitcnt lgkmcnt(3)
	v_cmp_gt_u64_e64 s[12:13], v[6:7], v[4:5]
	v_cmp_gt_u64_e64 s[100:101], v[8:9], v[4:5]
	s_nop 0
	v_cndmask_b32_e64 v6, 0, 1, s[12:13]
	v_addc_co_u32_e64 v3, s[100:101], v3, v6, s[100:101]
	s_waitcnt lgkmcnt(2)
	v_cmp_gt_u64_e64 s[12:13], v[14:15], v[4:5]
	v_cmp_gt_u64_e64 s[100:101], v[16:17], v[4:5]
	s_nop 0
	v_cndmask_b32_e64 v6, 0, 1, s[12:13]
	v_addc_co_u32_e64 v3, s[100:101], v3, v6, s[100:101]
	s_waitcnt lgkmcnt(1)
	v_cmp_gt_u64_e64 s[12:13], v[18:19], v[4:5]
	v_cmp_gt_u64_e64 s[100:101], v[20:21], v[4:5]
	s_nop 0
	v_cndmask_b32_e64 v6, 0, 1, s[12:13]
	v_addc_co_u32_e64 v3, s[100:101], v3, v6, s[100:101]
	s_waitcnt lgkmcnt(0)
	v_cmp_gt_u64_e64 s[12:13], v[22:23], v[4:5]
	v_cmp_gt_u64_e64 s[100:101], v[24:25], v[4:5]
	s_nop 0
	v_cndmask_b32_e64 v6, 0, 1, s[12:13]
	v_addc_co_u32_e64 v3, s[100:101], v3, v6, s[100:101]

; template <int NC> __device__ __forceinline__ void idx_rank(LAS unsigned long long* cc, int n, unsigned nd, int lane, LAS unsigned* mrow) {
;     ...
; #pragma unroll 2
;     for (int c2 = 0; c2 < n8; c2 += 8) {
;         unsigned long long a[8];
; #pragma unroll
;         for (int i = 0; i < 8; ++i) a[i] = cc[c2 + i];
; #pragma unroll
;         for (int i = 0; i < 8; ++i)
; #pragma unroll
;             for (int k = 0; k < NC; ++k) rank[k] += (a[i] > me[k]) ? 1u : 0u;
;     }
.LBB0_1417:
	s_lshl_b32 s0, s1, 3
	s_add_i32 s0, s19, s0
	v_mov_b32_e32 v9, s0
	ds_read_b128 v[14:17], v9 offset:512
	s_waitcnt vmcnt(3)
	ds_read_b128 v[18:21], v9 offset:528
	s_waitcnt vmcnt(2)
	ds_read_b128 v[22:25], v9 offset:544
	s_waitcnt vmcnt(1)
	ds_read_b128 v[26:29], v9 offset:560
	s_waitcnt lgkmcnt(3)
	v_cmp_gt_u64_e64 s[14:15], v[14:15], v[6:7]
	v_cmp_gt_u64_e64 s[100:101], v[14:15], v[4:5]
	s_nop 0
	v_cndmask_b32_e64 v9, 0, 1, s[14:15]
	v_cndmask_b32_e64 v13, 0, 1, s[100:101]
	v_cmp_gt_u64_e64 s[14:15], v[16:17], v[6:7]
	v_cmp_gt_u64_e64 s[100:101], v[16:17], v[4:5]
	s_nop 0
	v_addc_co_u32_e64 v8, s[14:15], v8, v9, s[14:15]
	v_addc_co_u32_e64 v3, s[100:101], v3, v13, s[100:101]
	s_waitcnt lgkmcnt(2)
	v_cmp_gt_u64_e64 s[14:15], v[18:19], v[6:7]
	v_cmp_gt_u64_e64 s[100:101], v[18:19], v[4:5]
	s_nop 0
	v_cndmask_b32_e64 v9, 0, 1, s[14:15]
	v_cndmask_b32_e64 v13, 0, 1, s[100:101]
	v_cmp_gt_u64_e64 s[14:15], v[20:21], v[6:7]
	v_cmp_gt_u64_e64 s[100:101], v[20:21], v[4:5]
	s_nop 0
	v_addc_co_u32_e64 v8, s[14:15], v8, v9, s[14:15]
	v_addc_co_u32_e64 v3, s[100:101], v3, v13, s[100:101]
	s_waitcnt lgkmcnt(1)
	v_cmp_gt_u64_e64 s[14:15], v[22:23], v[6:7]
	v_cmp_gt_u64_e64 s[100:101], v[22:23], v[4:5]
	s_nop 0
	v_cndmask_b32_e64 v9, 0, 1, s[14:15]
	v_cndmask_b32_e64 v13, 0, 1, s[100:101]
	v_cmp_gt_u64_e64 s[14:15], v[24:25], v[6:7]
	v_cmp_gt_u64_e64 s[100:101], v[24:25], v[4:5]
	s_nop 0
	v_addc_co_u32_e64 v8, s[14:15], v8, v9, s[14:15]
	v_addc_co_u32_e64 v3, s[100:101], v3, v13, s[100:101]
	s_waitcnt lgkmcnt(0)
	v_cmp_gt_u64_e64 s[14:15], v[26:27], v[6:7]
	v_cmp_gt_u64_e64 s[100:101], v[26:27], v[4:5]
	s_nop 0
	v_cndmask_b32_e64 v9, 0, 1, s[14:15]
	v_cndmask_b32_e64 v13, 0, 1, s[100:101]
	v_cmp_gt_u64_e64 s[14:15], v[28:29], v[6:7]
	v_cmp_gt_u64_e64 s[100:101], v[28:29], v[4:5]
	s_nop 0
	v_addc_co_u32_e64 v8, s[14:15], v8, v9, s[14:15]
	v_addc_co_u32_e64 v3, s[100:101], v3, v13, s[100:101]

; template <int NC> __device__ __forceinline__ void idx_rank(LAS unsigned long long* cc, int n, unsigned nd, int lane, LAS unsigned* mrow) {
;     ...
; #pragma unroll 2
;     for (int c2 = 0; c2 < n8; c2 += 8) {
;         unsigned long long a[8];
; #pragma unroll
;         for (int i = 0; i < 8; ++i) a[i] = cc[c2 + i];
; #pragma unroll
;         for (int i = 0; i < 8; ++i)
; #pragma unroll
;             for (int k = 0; k < NC; ++k) rank[k] += (a[i] > me[k]) ? 1u : 0u;
;     }
.LBB0_1424:
	s_lshl_b32 s1, s2, 3
	s_add_i32 s1, s21, s1
	v_mov_b32_e32 v15, s1
	s_waitcnt vmcnt(3)
	ds_read_b128 v[16:19], v15 offset:512
	s_waitcnt vmcnt(2)
	ds_read_b128 v[20:23], v15 offset:528
	s_waitcnt vmcnt(1)
	ds_read_b128 v[24:27], v15 offset:544
	s_waitcnt vmcnt(0)
	ds_read_b128 v[28:31], v15 offset:560
	s_waitcnt lgkmcnt(3)
	v_cmp_gt_u64_e64 s[16:17], v[16:17], v[8:9]
	v_cmp_gt_u64_e64 s[100:101], v[16:17], v[4:5]
	s_nop 0
	v_cndmask_b32_e64 v15, 0, 1, s[16:17]
	v_cndmask_b32_e64 v32, 0, 1, s[100:101]
	v_cmp_gt_u64_e64 s[16:17], v[16:17], v[6:7]
	v_cmp_gt_u64_e64 s[100:101], v[18:19], v[8:9]
	s_nop 0
	v_cndmask_b32_e64 v16, 0, 1, s[16:17]
	v_addc_co_u32_e64 v14, s[100:101], v14, v15, s[100:101]
	v_cmp_gt_u64_e64 s[16:17], v[18:19], v[4:5]
	v_cmp_gt_u64_e64 s[100:101], v[18:19], v[6:7]
	s_nop 0
	v_addc_co_u32_e64 v13, s[16:17], v13, v32, s[16:17]
	v_addc_co_u32_e64 v3, s[100:101], v3, v16, s[100:101]
	s_waitcnt lgkmcnt(2)
	v_cmp_gt_u64_e64 s[16:17], v[20:21], v[8:9]
	v_cmp_gt_u64_e64 s[100:101], v[20:21], v[4:5]
	s_nop 0
	v_cndmask_b32_e64 v15, 0, 1, s[16:17]
	v_cndmask_b32_e64 v16, 0, 1, s[100:101]
	v_cmp_gt_u64_e64 s[16:17], v[20:21], v[6:7]
	v_cmp_gt_u64_e64 s[100:101], v[22:23], v[8:9]
	s_nop 0
	v_cndmask_b32_e64 v17, 0, 1, s[16:17]
	v_addc_co_u32_e64 v14, s[100:101], v14, v15, s[100:101]
	v_cmp_gt_u64_e64 s[16:17], v[22:23], v[4:5]
	v_cmp_gt_u64_e64 s[100:101], v[22:23], v[6:7]
	s_nop 0
	v_addc_co_u32_e64 v13, s[16:17], v13, v16, s[16:17]
	v_addc_co_u32_e64 v3, s[100:101], v3, v17, s[100:101]
	s_waitcnt lgkmcnt(1)
	v_cmp_gt_u64_e64 s[16:17], v[24:25], v[8:9]
	v_cmp_gt_u64_e64 s[100:101], v[24:25], v[4:5]
	s_nop 0
	v_cndmask_b32_e64 v15, 0, 1, s[16:17]
	v_cndmask_b32_e64 v16, 0, 1, s[100:101]
	v_cmp_gt_u64_e64 s[16:17], v[24:25], v[6:7]
	v_cmp_gt_u64_e64 s[100:101], v[26:27], v[8:9]
	s_nop 0
	v_cndmask_b32_e64 v17, 0, 1, s[16:17]
	v_addc_co_u32_e64 v14, s[100:101], v14, v15, s[100:101]
	v_cmp_gt_u64_e64 s[16:17], v[26:27], v[4:5]
	v_cmp_gt_u64_e64 s[100:101], v[26:27], v[6:7]
	s_nop 0
	v_addc_co_u32_e64 v13, s[16:17], v13, v16, s[16:17]
	v_addc_co_u32_e64 v3, s[100:101], v3, v17, s[100:101]
	s_waitcnt lgkmcnt(0)
	v_cmp_gt_u64_e64 s[16:17], v[28:29], v[8:9]
	v_cmp_gt_u64_e64 s[100:101], v[28:29], v[4:5]
	s_nop 0
	v_cndmask_b32_e64 v15, 0, 1, s[16:17]
	v_cndmask_b32_e64 v16, 0, 1, s[100:101]
	v_cmp_gt_u64_e64 s[16:17], v[28:29], v[6:7]
	v_cmp_gt_u64_e64 s[100:101], v[30:31], v[8:9]
	s_nop 0
	v_cndmask_b32_e64 v17, 0, 1, s[16:17]
	v_addc_co_u32_e64 v14, s[100:101], v14, v15, s[100:101]
	v_cmp_gt_u64_e64 s[16:17], v[30:31], v[4:5]
	v_cmp_gt_u64_e64 s[100:101], v[30:31], v[6:7]
	s_nop 0
	v_addc_co_u32_e64 v13, s[16:17], v13, v16, s[16:17]
	v_addc_co_u32_e64 v3, s[100:101], v3, v17, s[100:101]

; template <int NC> __device__ __forceinline__ void idx_rank(LAS unsigned long long* cc, int n, unsigned nd, int lane, LAS unsigned* mrow) {
;     ...
; #pragma unroll 2
;     for (int c2 = 0; c2 < n8; c2 += 8) {
;         unsigned long long a[8];
; #pragma unroll
;         for (int i = 0; i < 8; ++i) a[i] = cc[c2 + i];
; #pragma unroll
;         for (int i = 0; i < 8; ++i)
; #pragma unroll
;             for (int k = 0; k < NC; ++k) rank[k] += (a[i] > me[k]) ? 1u : 0u;
;     }
.LBB0_1447:
	s_lshl_b32 s0, s1, 3
	s_add_i32 s0, s21, s0
	v_mov_b32_e32 v9, s0
	ds_read_b128 v[14:17], v9 offset:512
	s_waitcnt vmcnt(3)
	ds_read_b128 v[18:21], v9 offset:528
	s_waitcnt vmcnt(2)
	ds_read_b128 v[22:25], v9 offset:544
	s_waitcnt vmcnt(1)
	ds_read_b128 v[26:29], v9 offset:560
	s_waitcnt lgkmcnt(3)
	v_cmp_gt_u64_e64 s[14:15], v[14:15], v[6:7]
	v_cmp_gt_u64_e64 s[100:101], v[14:15], v[4:5]
	s_nop 0
	v_cndmask_b32_e64 v9, 0, 1, s[14:15]
	v_cndmask_b32_e64 v13, 0, 1, s[100:101]
	v_cmp_gt_u64_e64 s[14:15], v[16:17], v[6:7]
	v_cmp_gt_u64_e64 s[100:101], v[16:17], v[4:5]
	s_nop 0
	v_addc_co_u32_e64 v8, s[14:15], v8, v9, s[14:15]
	v_addc_co_u32_e64 v3, s[100:101], v3, v13, s[100:101]
	s_waitcnt lgkmcnt(2)
	v_cmp_gt_u64_e64 s[14:15], v[18:19], v[6:7]
	v_cmp_gt_u64_e64 s[100:101], v[18:19], v[4:5]
	s_nop 0
	v_cndmask_b32_e64 v9, 0, 1, s[14:15]
	v_cndmask_b32_e64 v13, 0, 1, s[100:101]
	v_cmp_gt_u64_e64 s[14:15], v[20:21], v[6:7]
	v_cmp_gt_u64_e64 s[100:101], v[20:21], v[4:5]
	s_nop 0
	v_addc_co_u32_e64 v8, s[14:15], v8, v9, s[14:15]
	v_addc_co_u32_e64 v3, s[100:101], v3, v13, s[100:101]
	s_waitcnt lgkmcnt(1)
	v_cmp_gt_u64_e64 s[14:15], v[22:23], v[6:7]
	v_cmp_gt_u64_e64 s[100:101], v[22:23], v[4:5]
	s_nop 0
	v_cndmask_b32_e64 v9, 0, 1, s[14:15]
	v_cndmask_b32_e64 v13, 0, 1, s[100:101]
	v_cmp_gt_u64_e64 s[14:15], v[24:25], v[6:7]
	v_cmp_gt_u64_e64 s[100:101], v[24:25], v[4:5]
	s_nop 0
	v_addc_co_u32_e64 v8, s[14:15], v8, v9, s[14:15]
	v_addc_co_u32_e64 v3, s[100:101], v3, v13, s[100:101]
	s_waitcnt lgkmcnt(0)
	v_cmp_gt_u64_e64 s[14:15], v[26:27], v[6:7]
	v_cmp_gt_u64_e64 s[100:101], v[26:27], v[4:5]
	s_nop 0
	v_cndmask_b32_e64 v9, 0, 1, s[14:15]
	v_cndmask_b32_e64 v13, 0, 1, s[100:101]
	v_cmp_gt_u64_e64 s[14:15], v[28:29], v[6:7]
	v_cmp_gt_u64_e64 s[100:101], v[28:29], v[4:5]
	s_nop 0
	v_addc_co_u32_e64 v8, s[14:15], v8, v9, s[14:15]
	v_addc_co_u32_e64 v3, s[100:101], v3, v13, s[100:101]

; template <int NC> __device__ __forceinline__ void idx_rank(LAS unsigned long long* cc, int n, unsigned nd, int lane, LAS unsigned* mrow) {
;     ...
; #pragma unroll 2
;     for (int c2 = 0; c2 < n8; c2 += 8) {
;         unsigned long long a[8];
; #pragma unroll
;         for (int i = 0; i < 8; ++i) a[i] = cc[c2 + i];
; #pragma unroll
;         for (int i = 0; i < 8; ++i)
; #pragma unroll
;             for (int k = 0; k < NC; ++k) rank[k] += (a[i] > me[k]) ? 1u : 0u;
;     }
.LBB0_1467:
	s_lshl_b32 s0, s1, 3
	s_add_i32 s0, s21, s0
	v_mov_b32_e32 v13, s0
	ds_read_b128 v[6:9], v13 offset:512
	ds_read_b128 v[14:17], v13 offset:528
	s_waitcnt vmcnt(3)
	ds_read_b128 v[18:21], v13 offset:544
	s_waitcnt vmcnt(2)
	ds_read_b128 v[22:25], v13 offset:560
	s_waitcnt lgkmcnt(3)
	v_cmp_gt_u64_e64 s[12:13], v[6:7], v[4:5]
	v_cmp_gt_u64_e64 s[100:101], v[8:9], v[4:5]
	s_nop 0
	v_cndmask_b32_e64 v6, 0, 1, s[12:13]
	v_addc_co_u32_e64 v3, s[100:101], v3, v6, s[100:101]
	s_waitcnt lgkmcnt(2)
	v_cmp_gt_u64_e64 s[12:13], v[14:15], v[4:5]
	v_cmp_gt_u64_e64 s[100:101], v[16:17], v[4:5]
	s_nop 0
	v_cndmask_b32_e64 v6, 0, 1, s[12:13]
	v_addc_co_u32_e64 v3, s[100:101], v3, v6, s[100:101]
	s_waitcnt lgkmcnt(1)
	v_cmp_gt_u64_e64 s[12:13], v[18:19], v[4:5]
	v_cmp_gt_u64_e64 s[100:101], v[20:21], v[4:5]
	s_nop 0
	v_cndmask_b32_e64 v6, 0, 1, s[12:13]
	v_addc_co_u32_e64 v3, s[100:101], v3, v6, s[100:101]
	s_waitcnt lgkmcnt(0)
	v_cmp_gt_u64_e64 s[12:13], v[22:23], v[4:5]
	v_cmp_gt_u64_e64 s[100:101], v[24:25], v[4:5]
	s_nop 0
	v_cndmask_b32_e64 v6, 0, 1, s[12:13]
	v_addc_co_u32_e64 v3, s[100:101], v3, v6, s[100:101]

; template <int NC> __device__ __forceinline__ void idx_rank(LAS unsigned long long* cc, int n, unsigned nd, int lane, LAS unsigned* mrow) {
;     ...
; #pragma unroll 2
;     for (int c2 = 0; c2 < n8; c2 += 8) {
;         unsigned long long a[8];
; #pragma unroll
;         for (int i = 0; i < 8; ++i) a[i] = cc[c2 + i];
; #pragma unroll
;         for (int i = 0; i < 8; ++i)
; #pragma unroll
;             for (int k = 0; k < NC; ++k) rank[k] += (a[i] > me[k]) ? 1u : 0u;
;     }
.LBB0_1574:
	s_waitcnt vmcnt(0)
	v_mov_b32_e32 v30, s33
	ds_read_b128 v[14:17], v30
	ds_read_b128 v[18:21], v30 offset:16
	ds_read_b128 v[22:25], v30 offset:32
	ds_read_b128 v[26:29], v30 offset:48
	s_add_i32 s2, s2, 16
	s_waitcnt lgkmcnt(3)
	s_addk_i32 s33, 0x80
	s_add_i32 s3, s3, -2
	s_cmp_lg_u32 s3, 0
	v_cmp_gt_u64_e64 s[16:17], v[14:15], v[8:9]
	v_cmp_gt_u64_e64 s[100:101], v[14:15], v[4:5]
	s_nop 0
	v_cndmask_b32_e64 v31, 0, 1, s[16:17]
	v_cndmask_b32_e64 v32, 0, 1, s[100:101]
	v_cmp_gt_u64_e64 s[16:17], v[14:15], v[6:7]
	v_cmp_gt_u64_e64 s[100:101], v[16:17], v[8:9]
	s_nop 0
	v_cndmask_b32_e64 v14, 0, 1, s[16:17]
	v_addc_co_u32_e64 v13, s[100:101], v13, v31, s[100:101]
	v_cmp_gt_u64_e64 s[16:17], v[16:17], v[4:5]
	v_cmp_gt_u64_e64 s[100:101], v[16:17], v[6:7]
	s_nop 0
	v_addc_co_u32_e64 v12, s[16:17], v12, v32, s[16:17]
	v_addc_co_u32_e64 v3, s[100:101], v3, v14, s[100:101]
	s_waitcnt lgkmcnt(2)
	v_cmp_gt_u64_e64 s[16:17], v[18:19], v[8:9]
	v_cmp_gt_u64_e64 s[100:101], v[18:19], v[4:5]
	s_nop 0
	v_cndmask_b32_e64 v14, 0, 1, s[16:17]
	v_cndmask_b32_e64 v15, 0, 1, s[100:101]
	v_cmp_gt_u64_e64 s[16:17], v[18:19], v[6:7]
	v_cmp_gt_u64_e64 s[100:101], v[20:21], v[8:9]
	s_nop 0
	v_cndmask_b32_e64 v16, 0, 1, s[16:17]
	v_addc_co_u32_e64 v13, s[100:101], v13, v14, s[100:101]
	v_cmp_gt_u64_e64 s[16:17], v[20:21], v[4:5]
	v_cmp_gt_u64_e64 s[100:101], v[20:21], v[6:7]
	s_nop 0
	v_addc_co_u32_e64 v12, s[16:17], v12, v15, s[16:17]
	v_addc_co_u32_e64 v3, s[100:101], v3, v16, s[100:101]
	s_waitcnt lgkmcnt(1)
	v_cmp_gt_u64_e64 s[16:17], v[22:23], v[8:9]
	v_cmp_gt_u64_e64 s[100:101], v[22:23], v[4:5]
	s_nop 0
	v_cndmask_b32_e64 v14, 0, 1, s[16:17]
	v_cndmask_b32_e64 v15, 0, 1, s[100:101]
	v_cmp_gt_u64_e64 s[16:17], v[22:23], v[6:7]
	v_cmp_gt_u64_e64 s[100:101], v[24:25], v[8:9]
	s_nop 0
	v_cndmask_b32_e64 v16, 0, 1, s[16:17]
	v_addc_co_u32_e64 v13, s[100:101], v13, v14, s[100:101]
	v_cmp_gt_u64_e64 s[16:17], v[24:25], v[4:5]
	v_cmp_gt_u64_e64 s[100:101], v[24:25], v[6:7]
	s_nop 0
	v_addc_co_u32_e64 v12, s[16:17], v12, v15, s[16:17]
	v_addc_co_u32_e64 v3, s[100:101], v3, v16, s[100:101]
	s_waitcnt lgkmcnt(0)
	v_cmp_gt_u64_e64 s[16:17], v[26:27], v[8:9]
	v_cmp_gt_u64_e64 s[100:101], v[26:27], v[4:5]
	s_nop 0
	v_cndmask_b32_e64 v14, 0, 1, s[16:17]
	v_cndmask_b32_e64 v15, 0, 1, s[100:101]
	v_cmp_gt_u64_e64 s[16:17], v[26:27], v[6:7]
	v_cmp_gt_u64_e64 s[100:101], v[28:29], v[8:9]
	s_nop 0
	v_cndmask_b32_e64 v16, 0, 1, s[16:17]
	v_addc_co_u32_e64 v31, s[100:101], v13, v14, s[100:101]
	v_cmp_gt_u64_e64 s[16:17], v[28:29], v[4:5]
	v_cmp_gt_u64_e64 s[100:101], v[28:29], v[6:7]
	s_nop 0
	v_addc_co_u32_e64 v32, s[16:17], v12, v15, s[16:17]
	v_addc_co_u32_e64 v3, s[100:101], v3, v16, s[100:101]
	ds_read_b128 v[12:15], v30 offset:64
	ds_read_b128 v[16:19], v30 offset:80
	ds_read_b128 v[20:23], v30 offset:96
	ds_read_b128 v[24:27], v30 offset:112
	s_waitcnt lgkmcnt(3)
	v_cmp_gt_u64_e64 s[16:17], v[12:13], v[8:9]
	v_cmp_gt_u64_e64 s[100:101], v[12:13], v[4:5]
	s_nop 0
	v_cndmask_b32_e64 v28, 0, 1, s[16:17]
	v_cndmask_b32_e64 v29, 0, 1, s[100:101]
	v_cmp_gt_u64_e64 s[16:17], v[12:13], v[6:7]
	v_cmp_gt_u64_e64 s[100:101], v[14:15], v[8:9]
	s_nop 0
	v_cndmask_b32_e64 v12, 0, 1, s[16:17]
	v_addc_co_u32_e64 v13, s[100:101], v31, v28, s[100:101]
	v_cmp_gt_u64_e64 s[16:17], v[14:15], v[4:5]
	v_cmp_gt_u64_e64 s[100:101], v[14:15], v[6:7]
	s_nop 0
	v_addc_co_u32_e64 v28, s[16:17], v32, v29, s[16:17]
	v_addc_co_u32_e64 v3, s[100:101], v3, v12, s[100:101]
	s_waitcnt lgkmcnt(2)
	v_cmp_gt_u64_e64 s[16:17], v[16:17], v[8:9]
	v_cmp_gt_u64_e64 s[100:101], v[16:17], v[4:5]
	s_nop 0
	v_cndmask_b32_e64 v12, 0, 1, s[16:17]
	v_cndmask_b32_e64 v14, 0, 1, s[100:101]
	v_cmp_gt_u64_e64 s[16:17], v[16:17], v[6:7]
	v_cmp_gt_u64_e64 s[100:101], v[18:19], v[8:9]
	s_nop 0
	v_cndmask_b32_e64 v15, 0, 1, s[16:17]
	v_addc_co_u32_e64 v12, s[100:101], v13, v12, s[100:101]
	v_cmp_gt_u64_e64 s[16:17], v[18:19], v[4:5]
	v_cmp_gt_u64_e64 s[100:101], v[18:19], v[6:7]
	s_nop 0
	v_addc_co_u32_e64 v13, s[16:17], v28, v14, s[16:17]
	v_addc_co_u32_e64 v3, s[100:101], v3, v15, s[100:101]
	s_waitcnt lgkmcnt(1)
	v_cmp_gt_u64_e64 s[16:17], v[20:21], v[8:9]
	v_cmp_gt_u64_e64 s[100:101], v[20:21], v[4:5]
	s_nop 0
	v_cndmask_b32_e64 v14, 0, 1, s[16:17]
	v_cndmask_b32_e64 v15, 0, 1, s[100:101]
	v_cmp_gt_u64_e64 s[16:17], v[20:21], v[6:7]
	v_cmp_gt_u64_e64 s[100:101], v[22:23], v[8:9]
	s_nop 0
	v_cndmask_b32_e64 v16, 0, 1, s[16:17]
	v_addc_co_u32_e64 v12, s[100:101], v12, v14, s[100:101]
	v_cmp_gt_u64_e64 s[16:17], v[22:23], v[4:5]
	v_cmp_gt_u64_e64 s[100:101], v[22:23], v[6:7]
	s_nop 0
	v_addc_co_u32_e64 v14, s[16:17], v13, v15, s[16:17]
	v_addc_co_u32_e64 v3, s[100:101], v3, v16, s[100:101]
	s_waitcnt lgkmcnt(0)
	v_cmp_gt_u64_e64 s[16:17], v[24:25], v[8:9]
	v_cmp_gt_u64_e64 s[100:101], v[24:25], v[4:5]
	s_nop 0
	v_cndmask_b32_e64 v13, 0, 1, s[16:17]
	v_cndmask_b32_e64 v15, 0, 1, s[100:101]
	v_cmp_gt_u64_e64 s[16:17], v[24:25], v[6:7]
	v_cmp_gt_u64_e64 s[100:101], v[26:27], v[8:9]
	s_nop 0
	v_cndmask_b32_e64 v16, 0, 1, s[16:17]
	v_addc_co_u32_e64 v13, s[100:101], v12, v13, s[100:101]
	v_cmp_gt_u64_e64 s[16:17], v[26:27], v[4:5]
	v_cmp_gt_u64_e64 s[100:101], v[26:27], v[6:7]
	s_nop 0
	v_addc_co_u32_e64 v12, s[16:17], v14, v15, s[16:17]
	v_addc_co_u32_e64 v3, s[100:101], v3, v16, s[100:101]
	s_cbranch_scc1 .LBB0_1574
	s_bitcmp1_b32 s1, 3
	s_cbranch_scc0 .LBB0_1578
	s_branch .LBB0_1579

; template <int NC> __device__ __forceinline__ void idx_rank(LAS unsigned long long* cc, int n, unsigned nd, int lane, LAS unsigned* mrow) {
;     ...
; #pragma unroll 2
;     for (int c2 = 0; c2 < n8; c2 += 8) {
;         unsigned long long a[8];
; #pragma unroll
;         for (int i = 0; i < 8; ++i) a[i] = cc[c2 + i];
; #pragma unroll
;         for (int i = 0; i < 8; ++i)
; #pragma unroll
;             for (int k = 0; k < NC; ++k) rank[k] += (a[i] > me[k]) ? 1u : 0u;
;     }
.LBB0_1578:
	s_lshl_b32 s1, s2, 3
	s_add_i32 s1, s18, s1
	s_waitcnt vmcnt(1)
	v_mov_b32_e32 v26, s1
	ds_read_b128 v[14:17], v26 offset:512
	ds_read_b128 v[18:21], v26 offset:528
	ds_read_b128 v[22:25], v26 offset:544
	ds_read_b128 v[26:29], v26 offset:560
	s_waitcnt lgkmcnt(3)
	s_waitcnt vmcnt(0)
	v_cmp_gt_u64_e64 s[16:17], v[14:15], v[8:9]
	v_cmp_gt_u64_e64 s[100:101], v[14:15], v[4:5]
	s_nop 0
	v_cndmask_b32_e64 v30, 0, 1, s[16:17]
	v_cndmask_b32_e64 v31, 0, 1, s[100:101]
	v_cmp_gt_u64_e64 s[16:17], v[14:15], v[6:7]
	v_cmp_gt_u64_e64 s[100:101], v[16:17], v[8:9]
	s_nop 0
	v_cndmask_b32_e64 v14, 0, 1, s[16:17]
	v_addc_co_u32_e64 v13, s[100:101], v13, v30, s[100:101]
	v_cmp_gt_u64_e64 s[16:17], v[16:17], v[4:5]
	v_cmp_gt_u64_e64 s[100:101], v[16:17], v[6:7]
	s_nop 0
	v_addc_co_u32_e64 v12, s[16:17], v12, v31, s[16:17]
	v_addc_co_u32_e64 v3, s[100:101], v3, v14, s[100:101]
	s_waitcnt lgkmcnt(2)
	v_cmp_gt_u64_e64 s[16:17], v[18:19], v[8:9]
	v_cmp_gt_u64_e64 s[100:101], v[18:19], v[4:5]
	s_nop 0
	v_cndmask_b32_e64 v14, 0, 1, s[16:17]
	v_cndmask_b32_e64 v15, 0, 1, s[100:101]
	v_cmp_gt_u64_e64 s[16:17], v[18:19], v[6:7]
	v_cmp_gt_u64_e64 s[100:101], v[20:21], v[8:9]
	s_nop 0
	v_cndmask_b32_e64 v16, 0, 1, s[16:17]
	v_addc_co_u32_e64 v13, s[100:101], v13, v14, s[100:101]
	v_cmp_gt_u64_e64 s[16:17], v[20:21], v[4:5]
	v_cmp_gt_u64_e64 s[100:101], v[20:21], v[6:7]
	s_nop 0
	v_addc_co_u32_e64 v12, s[16:17], v12, v15, s[16:17]
	v_addc_co_u32_e64 v3, s[100:101], v3, v16, s[100:101]
	s_waitcnt lgkmcnt(1)
	v_cmp_gt_u64_e64 s[16:17], v[22:23], v[8:9]
	v_cmp_gt_u64_e64 s[100:101], v[22:23], v[4:5]
	s_nop 0
	v_cndmask_b32_e64 v14, 0, 1, s[16:17]
	v_cndmask_b32_e64 v15, 0, 1, s[100:101]
	v_cmp_gt_u64_e64 s[16:17], v[22:23], v[6:7]
	v_cmp_gt_u64_e64 s[100:101], v[24:25], v[8:9]
	s_nop 0
	v_cndmask_b32_e64 v16, 0, 1, s[16:17]
	v_addc_co_u32_e64 v13, s[100:101], v13, v14, s[100:101]
	v_cmp_gt_u64_e64 s[16:17], v[24:25], v[4:5]
	v_cmp_gt_u64_e64 s[100:101], v[24:25], v[6:7]
	s_nop 0
	v_addc_co_u32_e64 v12, s[16:17], v12, v15, s[16:17]
	v_addc_co_u32_e64 v3, s[100:101], v3, v16, s[100:101]
	s_waitcnt lgkmcnt(0)
	v_cmp_gt_u64_e64 s[16:17], v[26:27], v[8:9]
	v_cmp_gt_u64_e64 s[100:101], v[26:27], v[4:5]
	s_nop 0
	v_cndmask_b32_e64 v14, 0, 1, s[16:17]
	v_cndmask_b32_e64 v15, 0, 1, s[100:101]
	v_cmp_gt_u64_e64 s[16:17], v[26:27], v[6:7]
	v_cmp_gt_u64_e64 s[100:101], v[28:29], v[8:9]
	s_nop 0
	v_cndmask_b32_e64 v16, 0, 1, s[16:17]
	v_addc_co_u32_e64 v13, s[100:101], v13, v14, s[100:101]
	v_cmp_gt_u64_e64 s[16:17], v[28:29], v[4:5]
	v_cmp_gt_u64_e64 s[100:101], v[28:29], v[6:7]
	s_nop 0
	v_addc_co_u32_e64 v12, s[16:17], v12, v15, s[16:17]
	v_addc_co_u32_e64 v3, s[100:101], v3, v16, s[100:101]

; template <int NC> __device__ __forceinline__ void idx_rank(LAS unsigned long long* cc, int n, unsigned nd, int lane, LAS unsigned* mrow) {
;     ...
; #pragma unroll 2
;     for (int c2 = 0; c2 < n8; c2 += 8) {
;         unsigned long long a[8];
; #pragma unroll
;         for (int i = 0; i < 8; ++i) a[i] = cc[c2 + i];
; #pragma unroll
;         for (int i = 0; i < 8; ++i)
; #pragma unroll
;             for (int k = 0; k < NC; ++k) rank[k] += (a[i] > me[k]) ? 1u : 0u;
;     }
.LBB0_1595:
	v_mov_b32_e32 v9, s3
	ds_read_b128 v[12:15], v9
	s_waitcnt vmcnt(3)
	ds_read_b128 v[16:19], v9 offset:16
	s_waitcnt vmcnt(2)
	ds_read_b128 v[20:23], v9 offset:32
	s_waitcnt vmcnt(1)
	ds_read_b128 v[24:27], v9 offset:48
	s_add_i32 s1, s1, 16
	s_waitcnt lgkmcnt(3)
	s_addk_i32 s3, 0x80
	s_add_i32 s2, s2, -2
	s_cmp_lg_u32 s2, 0
	v_cmp_gt_u64_e64 s[14:15], v[12:13], v[6:7]
	v_cmp_gt_u64_e64 s[100:101], v[12:13], v[4:5]
	s_nop 0
	v_cndmask_b32_e64 v11, 0, 1, s[14:15]
	v_cndmask_b32_e64 v12, 0, 1, s[100:101]
	v_cmp_gt_u64_e64 s[14:15], v[14:15], v[6:7]
	v_cmp_gt_u64_e64 s[100:101], v[14:15], v[4:5]
	s_nop 0
	v_addc_co_u32_e64 v8, s[14:15], v8, v11, s[14:15]
	v_addc_co_u32_e64 v3, s[100:101], v3, v12, s[100:101]
	s_waitcnt lgkmcnt(2)
	v_cmp_gt_u64_e64 s[14:15], v[16:17], v[6:7]
	v_cmp_gt_u64_e64 s[100:101], v[16:17], v[4:5]
	s_nop 0
	v_cndmask_b32_e64 v11, 0, 1, s[14:15]
	v_cndmask_b32_e64 v12, 0, 1, s[100:101]
	v_cmp_gt_u64_e64 s[14:15], v[18:19], v[6:7]
	v_cmp_gt_u64_e64 s[100:101], v[18:19], v[4:5]
	s_nop 0
	v_addc_co_u32_e64 v8, s[14:15], v8, v11, s[14:15]
	v_addc_co_u32_e64 v3, s[100:101], v3, v12, s[100:101]
	s_waitcnt lgkmcnt(1)
	v_cmp_gt_u64_e64 s[14:15], v[20:21], v[6:7]
	v_cmp_gt_u64_e64 s[100:101], v[20:21], v[4:5]
	s_nop 0
	v_cndmask_b32_e64 v11, 0, 1, s[14:15]
	v_cndmask_b32_e64 v12, 0, 1, s[100:101]
	v_cmp_gt_u64_e64 s[14:15], v[22:23], v[6:7]
	v_cmp_gt_u64_e64 s[100:101], v[22:23], v[4:5]
	s_nop 0
	v_addc_co_u32_e64 v8, s[14:15], v8, v11, s[14:15]
	v_addc_co_u32_e64 v3, s[100:101], v3, v12, s[100:101]
	s_waitcnt lgkmcnt(0)
	v_cmp_gt_u64_e64 s[14:15], v[24:25], v[6:7]
	v_cmp_gt_u64_e64 s[100:101], v[24:25], v[4:5]
	s_nop 0
	v_cndmask_b32_e64 v11, 0, 1, s[14:15]
	v_cndmask_b32_e64 v12, 0, 1, s[100:101]
	v_cmp_gt_u64_e64 s[14:15], v[26:27], v[6:7]
	v_cmp_gt_u64_e64 s[100:101], v[26:27], v[4:5]
	s_nop 0
	v_addc_co_u32_e64 v8, s[14:15], v8, v11, s[14:15]
	v_addc_co_u32_e64 v3, s[100:101], v3, v12, s[100:101]
	ds_read_b128 v[12:15], v9 offset:64
	ds_read_b128 v[16:19], v9 offset:80
	ds_read_b128 v[20:23], v9 offset:96
	ds_read_b128 v[24:27], v9 offset:112
	s_waitcnt lgkmcnt(3)
	v_cmp_gt_u64_e64 s[14:15], v[12:13], v[6:7]
	v_cmp_gt_u64_e64 s[100:101], v[12:13], v[4:5]
	s_nop 0
	v_cndmask_b32_e64 v9, 0, 1, s[14:15]
	v_cndmask_b32_e64 v11, 0, 1, s[100:101]
	v_cmp_gt_u64_e64 s[14:15], v[14:15], v[6:7]
	v_cmp_gt_u64_e64 s[100:101], v[14:15], v[4:5]
	s_nop 0
	v_addc_co_u32_e64 v8, s[14:15], v8, v9, s[14:15]
	v_addc_co_u32_e64 v3, s[100:101], v3, v11, s[100:101]
	s_waitcnt lgkmcnt(2)
	v_cmp_gt_u64_e64 s[14:15], v[16:17], v[6:7]
	v_cmp_gt_u64_e64 s[100:101], v[16:17], v[4:5]
	s_nop 0
	v_cndmask_b32_e64 v9, 0, 1, s[14:15]
	v_cndmask_b32_e64 v11, 0, 1, s[100:101]
	v_cmp_gt_u64_e64 s[14:15], v[18:19], v[6:7]
	v_cmp_gt_u64_e64 s[100:101], v[18:19], v[4:5]
	s_nop 0
	v_addc_co_u32_e64 v8, s[14:15], v8, v9, s[14:15]
	v_addc_co_u32_e64 v3, s[100:101], v3, v11, s[100:101]
	s_waitcnt lgkmcnt(1)
	v_cmp_gt_u64_e64 s[14:15], v[20:21], v[6:7]
	v_cmp_gt_u64_e64 s[100:101], v[20:21], v[4:5]
	s_nop 0
	v_cndmask_b32_e64 v9, 0, 1, s[14:15]
	v_cndmask_b32_e64 v11, 0, 1, s[100:101]
	v_cmp_gt_u64_e64 s[14:15], v[22:23], v[6:7]
	v_cmp_gt_u64_e64 s[100:101], v[22:23], v[4:5]
	s_nop 0
	v_addc_co_u32_e64 v8, s[14:15], v8, v9, s[14:15]
	v_addc_co_u32_e64 v3, s[100:101], v3, v11, s[100:101]
	s_waitcnt lgkmcnt(0)
	v_cmp_gt_u64_e64 s[14:15], v[24:25], v[6:7]
	v_cmp_gt_u64_e64 s[100:101], v[24:25], v[4:5]
	s_nop 0
	v_cndmask_b32_e64 v9, 0, 1, s[14:15]
	v_cndmask_b32_e64 v11, 0, 1, s[100:101]
	v_cmp_gt_u64_e64 s[14:15], v[26:27], v[6:7]
	v_cmp_gt_u64_e64 s[100:101], v[26:27], v[4:5]
	s_nop 0
	v_addc_co_u32_e64 v8, s[14:15], v8, v9, s[14:15]
	v_addc_co_u32_e64 v3, s[100:101], v3, v11, s[100:101]
	s_cbranch_scc1 .LBB0_1595
	s_bitcmp1_b32 s0, 3
	s_cbranch_scc0 .LBB0_1601
	s_branch .LBB0_1602

; template <int NC> __device__ __forceinline__ void idx_rank(LAS unsigned long long* cc, int n, unsigned nd, int lane, LAS unsigned* mrow) {
;     ...
; #pragma unroll 2
;     for (int c2 = 0; c2 < n8; c2 += 8) {
;         unsigned long long a[8];
; #pragma unroll
;         for (int i = 0; i < 8; ++i) a[i] = cc[c2 + i];
; #pragma unroll
;         for (int i = 0; i < 8; ++i)
; #pragma unroll
;             for (int k = 0; k < NC; ++k) rank[k] += (a[i] > me[k]) ? 1u : 0u;
;     }
.LBB0_1601:
	s_lshl_b32 s0, s1, 3
	s_add_i32 s0, s18, s0
	v_mov_b32_e32 v9, s0
	ds_read_b128 v[12:15], v9 offset:512
	s_waitcnt vmcnt(3)
	ds_read_b128 v[16:19], v9 offset:528
	s_waitcnt vmcnt(2)
	ds_read_b128 v[20:23], v9 offset:544
	s_waitcnt vmcnt(1)
	ds_read_b128 v[24:27], v9 offset:560
	s_waitcnt lgkmcnt(3)
	v_cmp_gt_u64_e64 s[14:15], v[12:13], v[6:7]
	v_cmp_gt_u64_e64 s[100:101], v[12:13], v[4:5]
	s_nop 0
	v_cndmask_b32_e64 v9, 0, 1, s[14:15]
	v_cndmask_b32_e64 v11, 0, 1, s[100:101]
	v_cmp_gt_u64_e64 s[14:15], v[14:15], v[6:7]
	v_cmp_gt_u64_e64 s[100:101], v[14:15], v[4:5]
	s_nop 0
	v_addc_co_u32_e64 v8, s[14:15], v8, v9, s[14:15]
	v_addc_co_u32_e64 v3, s[100:101], v3, v11, s[100:101]
	s_waitcnt lgkmcnt(2)
	v_cmp_gt_u64_e64 s[14:15], v[16:17], v[6:7]
	v_cmp_gt_u64_e64 s[100:101], v[16:17], v[4:5]
	s_nop 0
	v_cndmask_b32_e64 v9, 0, 1, s[14:15]
	v_cndmask_b32_e64 v11, 0, 1, s[100:101]
	v_cmp_gt_u64_e64 s[14:15], v[18:19], v[6:7]
	v_cmp_gt_u64_e64 s[100:101], v[18:19], v[4:5]
	s_nop 0
	v_addc_co_u32_e64 v8, s[14:15], v8, v9, s[14:15]
	v_addc_co_u32_e64 v3, s[100:101], v3, v11, s[100:101]
	s_waitcnt lgkmcnt(1)
	v_cmp_gt_u64_e64 s[14:15], v[20:21], v[6:7]
	v_cmp_gt_u64_e64 s[100:101], v[20:21], v[4:5]
	s_nop 0
	v_cndmask_b32_e64 v9, 0, 1, s[14:15]
	v_cndmask_b32_e64 v11, 0, 1, s[100:101]
	v_cmp_gt_u64_e64 s[14:15], v[22:23], v[6:7]
	v_cmp_gt_u64_e64 s[100:101], v[22:23], v[4:5]
	s_nop 0
	v_addc_co_u32_e64 v8, s[14:15], v8, v9, s[14:15]
	v_addc_co_u32_e64 v3, s[100:101], v3, v11, s[100:101]
	s_waitcnt lgkmcnt(0)
	v_cmp_gt_u64_e64 s[14:15], v[24:25], v[6:7]
	v_cmp_gt_u64_e64 s[100:101], v[24:25], v[4:5]
	s_nop 0
	v_cndmask_b32_e64 v9, 0, 1, s[14:15]
	v_cndmask_b32_e64 v11, 0, 1, s[100:101]
	v_cmp_gt_u64_e64 s[14:15], v[26:27], v[6:7]
	v_cmp_gt_u64_e64 s[100:101], v[26:27], v[4:5]
	s_nop 0
	v_addc_co_u32_e64 v8, s[14:15], v8, v9, s[14:15]
	v_addc_co_u32_e64 v3, s[100:101], v3, v11, s[100:101]

; template <int NC> __device__ __forceinline__ void idx_rank(LAS unsigned long long* cc, int n, unsigned nd, int lane, LAS unsigned* mrow) {
;     ...
; #pragma unroll 2
;     for (int c2 = 0; c2 < n8; c2 += 8) {
;         unsigned long long a[8];
; #pragma unroll
;         for (int i = 0; i < 8; ++i) a[i] = cc[c2 + i];
; #pragma unroll
;         for (int i = 0; i < 8; ++i)
; #pragma unroll
;             for (int k = 0; k < NC; ++k) rank[k] += (a[i] > me[k]) ? 1u : 0u;
;     }
.LBB0_1617:
	v_mov_b32_e32 v11, s3
	ds_read_b128 v[6:9], v11
	ds_read_b128 v[12:15], v11 offset:16
	s_waitcnt vmcnt(3)
	ds_read_b128 v[16:19], v11 offset:32
	s_waitcnt vmcnt(2)
	ds_read_b128 v[20:23], v11 offset:48
	s_add_i32 s1, s1, 16
	s_waitcnt lgkmcnt(3)
	s_addk_i32 s3, 0x80
	s_add_i32 s2, s2, -2
	s_cmp_lg_u32 s2, 0
	v_cmp_gt_u64_e64 s[10:11], v[6:7], v[4:5]
	v_cmp_gt_u64_e64 s[100:101], v[8:9], v[4:5]
	s_nop 0
	v_cndmask_b32_e64 v6, 0, 1, s[10:11]
	v_addc_co_u32_e64 v3, s[100:101], v3, v6, s[100:101]
	s_waitcnt lgkmcnt(2)
	v_cmp_gt_u64_e64 s[10:11], v[12:13], v[4:5]
	v_cmp_gt_u64_e64 s[100:101], v[14:15], v[4:5]
	s_nop 0
	v_cndmask_b32_e64 v6, 0, 1, s[10:11]
	v_addc_co_u32_e64 v3, s[100:101], v3, v6, s[100:101]
	s_waitcnt lgkmcnt(1)
	v_cmp_gt_u64_e64 s[10:11], v[16:17], v[4:5]
	v_cmp_gt_u64_e64 s[100:101], v[18:19], v[4:5]
	s_nop 0
	v_cndmask_b32_e64 v6, 0, 1, s[10:11]
	v_addc_co_u32_e64 v3, s[100:101], v3, v6, s[100:101]
	s_waitcnt lgkmcnt(0)
	v_cmp_gt_u64_e64 s[10:11], v[20:21], v[4:5]
	v_cmp_gt_u64_e64 s[100:101], v[22:23], v[4:5]
	s_nop 0
	v_cndmask_b32_e64 v6, 0, 1, s[10:11]
	v_addc_co_u32_e64 v3, s[100:101], v3, v6, s[100:101]
	ds_read_b128 v[6:9], v11 offset:64
	ds_read_b128 v[12:15], v11 offset:80
	ds_read_b128 v[16:19], v11 offset:96
	ds_read_b128 v[20:23], v11 offset:112
	s_waitcnt lgkmcnt(3)
	v_cmp_gt_u64_e64 s[10:11], v[6:7], v[4:5]
	v_cmp_gt_u64_e64 s[100:101], v[8:9], v[4:5]
	s_nop 0
	v_cndmask_b32_e64 v6, 0, 1, s[10:11]
	v_addc_co_u32_e64 v3, s[100:101], v3, v6, s[100:101]
	s_waitcnt lgkmcnt(2)
	v_cmp_gt_u64_e64 s[10:11], v[12:13], v[4:5]
	v_cmp_gt_u64_e64 s[100:101], v[14:15], v[4:5]
	s_nop 0
	v_cndmask_b32_e64 v6, 0, 1, s[10:11]
	v_addc_co_u32_e64 v3, s[100:101], v3, v6, s[100:101]
	s_waitcnt lgkmcnt(1)
	v_cmp_gt_u64_e64 s[10:11], v[16:17], v[4:5]
	v_cmp_gt_u64_e64 s[100:101], v[18:19], v[4:5]
	s_nop 0
	v_cndmask_b32_e64 v6, 0, 1, s[10:11]
	v_addc_co_u32_e64 v3, s[100:101], v3, v6, s[100:101]
	s_waitcnt lgkmcnt(0)
	v_cmp_gt_u64_e64 s[10:11], v[20:21], v[4:5]
	v_cmp_gt_u64_e64 s[100:101], v[22:23], v[4:5]
	s_nop 0
	v_cndmask_b32_e64 v6, 0, 1, s[10:11]
	v_addc_co_u32_e64 v3, s[100:101], v3, v6, s[100:101]
	s_cbranch_scc1 .LBB0_1617
	s_bitcmp1_b32 s0, 3
	s_cbranch_scc0 .LBB0_1621
	s_branch .LBB0_1622

; template <int NC> __device__ __forceinline__ void idx_rank(LAS unsigned long long* cc, int n, unsigned nd, int lane, LAS unsigned* mrow) {
;     ...
; #pragma unroll 2
;     for (int c2 = 0; c2 < n8; c2 += 8) {
;         unsigned long long a[8];
; #pragma unroll
;         for (int i = 0; i < 8; ++i) a[i] = cc[c2 + i];
; #pragma unroll
;         for (int i = 0; i < 8; ++i)
; #pragma unroll
;             for (int k = 0; k < NC; ++k) rank[k] += (a[i] > me[k]) ? 1u : 0u;
;     }
.LBB0_1621:
	s_lshl_b32 s0, s1, 3
	s_add_i32 s0, s18, s0
	v_mov_b32_e32 v11, s0
	ds_read_b128 v[6:9], v11 offset:512
	ds_read_b128 v[12:15], v11 offset:528
	s_waitcnt vmcnt(3)
	ds_read_b128 v[16:19], v11 offset:544
	s_waitcnt vmcnt(2)
	ds_read_b128 v[20:23], v11 offset:560
	s_waitcnt lgkmcnt(3)
	v_cmp_gt_u64_e64 s[10:11], v[6:7], v[4:5]
	v_cmp_gt_u64_e64 s[100:101], v[8:9], v[4:5]
	s_nop 0
	v_cndmask_b32_e64 v6, 0, 1, s[10:11]
	v_addc_co_u32_e64 v3, s[100:101], v3, v6, s[100:101]
	s_waitcnt lgkmcnt(2)
	v_cmp_gt_u64_e64 s[10:11], v[12:13], v[4:5]
	v_cmp_gt_u64_e64 s[100:101], v[14:15], v[4:5]
	s_nop 0
	v_cndmask_b32_e64 v6, 0, 1, s[10:11]
	v_addc_co_u32_e64 v3, s[100:101], v3, v6, s[100:101]
	s_waitcnt lgkmcnt(1)
	v_cmp_gt_u64_e64 s[10:11], v[16:17], v[4:5]
	v_cmp_gt_u64_e64 s[100:101], v[18:19], v[4:5]
	s_nop 0
	v_cndmask_b32_e64 v6, 0, 1, s[10:11]
	v_addc_co_u32_e64 v3, s[100:101], v3, v6, s[100:101]
	s_waitcnt lgkmcnt(0)
	v_cmp_gt_u64_e64 s[10:11], v[20:21], v[4:5]
	v_cmp_gt_u64_e64 s[100:101], v[22:23], v[4:5]
	s_nop 0
	v_cndmask_b32_e64 v6, 0, 1, s[10:11]
	v_addc_co_u32_e64 v3, s[100:101], v3, v6, s[100:101]

; __global__ void __launch_bounds__(512, 2) trunk_fwd(Args args) {
	.amdhsa_kernel _Z9trunk_fwd4Args
		.amdhsa_group_segment_fixed_size 0
		.amdhsa_private_segment_fixed_size 0
		.amdhsa_kernarg_size 384
		.amdhsa_user_sgpr_count 2
		.amdhsa_user_sgpr_dispatch_ptr 0
		.amdhsa_user_sgpr_queue_ptr 0
		.amdhsa_user_sgpr_kernarg_segment_ptr 1
		.amdhsa_user_sgpr_dispatch_id 0
		.amdhsa_user_sgpr_kernarg_preload_length 0
		.amdhsa_user_sgpr_kernarg_preload_offset 0
		.amdhsa_user_sgpr_private_segment_size 0
		.amdhsa_uses_dynamic_stack 0
		.amdhsa_enable_private_segment 0
		.amdhsa_system_sgpr_workgroup_id_x 1
		.amdhsa_system_sgpr_workgroup_id_y 0
		.amdhsa_system_sgpr_workgroup_id_z 0
		.amdhsa_system_sgpr_workgroup_info 0
		.amdhsa_system_vgpr_workitem_id 0
		.amdhsa_next_free_vgpr 256
		.amdhsa_next_free_sgpr 102
		.amdhsa_accum_offset 256
		.amdhsa_reserve_vcc 1
		.amdhsa_float_round_mode_32 0
		.amdhsa_float_round_mode_16_64 0
		.amdhsa_float_denorm_mode_32 3
		.amdhsa_float_denorm_mode_16_64 3
		.amdhsa_dx10_clamp 1
		.amdhsa_ieee_mode 1
		.amdhsa_fp16_overflow 0
		.amdhsa_tg_split 0
		.amdhsa_exception_fp_ieee_invalid_op 0
		.amdhsa_exception_fp_denorm_src 0
		.amdhsa_exception_fp_ieee_div_zero 0
		.amdhsa_exception_fp_ieee_overflow 0
		.amdhsa_exception_fp_ieee_underflow 0
		.amdhsa_exception_fp_ieee_inexact 0
		.amdhsa_exception_int_div_zero 0
	.end_amdhsa_kernel

; __global__ void __launch_bounds__(512, 2) trunk_fwd(Args args) {
.Lfunc_end0:
	.size	_Z9trunk_fwd4Args, .Lfunc_end0-_Z9trunk_fwd4Args
	.set _Z9trunk_fwd4Args.num_vgpr, 256
	.set _Z9trunk_fwd4Args.num_agpr, 0
	.set _Z9trunk_fwd4Args.numbered_sgpr, 102
	.set _Z9trunk_fwd4Args.num_named_barrier, 0
	.set _Z9trunk_fwd4Args.private_seg_size, 0
	.set _Z9trunk_fwd4Args.uses_vcc, 1
	.set _Z9trunk_fwd4Args.uses_flat_scratch, 0
	.set _Z9trunk_fwd4Args.has_dyn_sized_stack, 0
	.set _Z9trunk_fwd4Args.has_recursion, 0
	.set _Z9trunk_fwd4Args.has_indirect_call, 0

; __global__ void __launch_bounds__(512, 2) trunk_fwd(Args args) {
amdhsa.kernels:
  - .agpr_count:     0
    .args:
      - .offset:         0
        .size:           128
        .value_kind:     by_value
      - .offset:         128
        .size:           4
        .value_kind:     hidden_block_count_x
      - .offset:         132
        .size:           4
        .value_kind:     hidden_block_count_y
      - .offset:         136
        .size:           4
        .value_kind:     hidden_block_count_z
      - .offset:         140
        .size:           2
        .value_kind:     hidden_group_size_x
      - .offset:         142
        .size:           2
        .value_kind:     hidden_group_size_y
      - .offset:         144
        .size:           2
        .value_kind:     hidden_group_size_z
      - .offset:         146
        .size:           2
        .value_kind:     hidden_remainder_x
      - .offset:         148
        .size:           2
        .value_kind:     hidden_remainder_y
      - .offset:         150
        .size:           2
        .value_kind:     hidden_remainder_z
      - .offset:         168
        .size:           8
        .value_kind:     hidden_global_offset_x
      - .offset:         176
        .size:           8
        .value_kind:     hidden_global_offset_y
      - .offset:         184
        .size:           8
        .value_kind:     hidden_global_offset_z
      - .offset:         192
        .size:           2
        .value_kind:     hidden_grid_dims
      - .offset:         248
        .size:           4
        .value_kind:     hidden_dynamic_lds_size
    .group_segment_fixed_size: 0
    .kernarg_segment_align: 8
    .kernarg_segment_size: 384
    .language:       OpenCL C
    .language_version:
      - 2
      - 0
    .max_flat_workgroup_size: 512
    .name:           _Z9trunk_fwd4Args
    .private_segment_fixed_size: 0
    .sgpr_count:     108
    .sgpr_spill_count: 100
    .symbol:         _Z9trunk_fwd4Args.kd
    .uniform_work_group_size: 1
    .uses_dynamic_stack: false
    .vgpr_count:     256
    .vgpr_spill_count: 0
    .wavefront_size: 64
